# differential attention rewritten by hand: one pass per (b,h,c) computes QK^T and softmax once and applies P to both 128-col V halves (was recomputed per half); K/V staged by LDS-DMA; bf16 MFMA f32 acc
# speedup vs baseline: 1.1003x; 1.1003x over previous
.Lfa_entry:
	s_waitcnt lgkmcnt(0)
	s_load_dwordx2 s[0:1], s[30:31], 0xd8
	v_mbcnt_lo_u32_b32 v0, -1, 0
	v_mbcnt_hi_u32_b32 v0, -1, v0
	s_lshr_b32 s15, s3, 6
	s_lshl_b32 s20, s15, 10
	s_mul_i32 s21, s15, 0xc00
	s_add_i32 s21, s21, 0x18800
	v_lshlrev_b32_e32 v1, 2, v0
	v_add_u32_e32 v1, s21, v1
	ds_write_b32 v1, v162 offset:0
	ds_write_b32 v1, v163 offset:256
	ds_write_b32 v1, v164 offset:512
	ds_write_b32 v1, v165 offset:768
	ds_write_b32 v1, v166 offset:1024
	ds_write_b32 v1, v167 offset:1280
	ds_write_b32 v1, v168 offset:1536
	ds_write_b32 v1, v169 offset:1792
	ds_write_b32 v1, v170 offset:2048
	ds_write_b32 v1, v171 offset:2304
	ds_write_b32 v1, v172 offset:2560
	ds_write_b32 v1, v173 offset:2816
	v_and_b32_e32 v2, 31, v0
	v_lshrrev_b32_e32 v3, 5, v0
	v_lshlrev_b32_e32 v208, 8, v2
	v_and_b32_e32 v4, 7, v2
	v_lshlrev_b32_e32 v4, 4, v4
	v_lshlrev_b32_e32 v5, 4, v3
	v_xor_b32_e32 v209, v4, v5
	v_and_b32_e32 v4, 3, v0
	v_lshlrev_b32_e32 v4, 3, v4
	v_bfe_u32 v5, v0, 2, 2
	v_lshl_or_b32 v4, v5, 6, v4
	v_bfe_u32 v5, v0, 4, 1
	v_lshl_or_b32 v4, v5, 5, v4
	v_lshl_or_b32 v210, v3, 8, v4
	v_lshrrev_b32_e32 v4, 4, v0
	v_and_b32_e32 v5, 15, v0
	s_add_i32 s21, s15, 0
	s_lshl_b32 s21, s21, 2
	v_add_u32_e32 v6, s21, v4
	v_and_b32_e32 v7, 7, v6
	v_xor_b32_e32 v7, v5, v7
	v_lshlrev_b32_e32 v7, 4, v7
	v_lshl_or_b32 v203, v6, 8, v7
	s_add_i32 s21, s15, 8
	s_lshl_b32 s21, s21, 2
	v_add_u32_e32 v6, s21, v4
	v_and_b32_e32 v7, 7, v6
	v_xor_b32_e32 v7, v5, v7
	v_lshlrev_b32_e32 v7, 4, v7
	v_lshl_or_b32 v204, v6, 8, v7
	v_bfe_u32 v4, v0, 2, 3
	v_and_b32_e32 v5, 3, v0
	v_lshlrev_b32_e32 v5, 4, v5
	s_add_i32 s21, s15, 0
	s_lshl_b32 s21, s21, 1
	v_add_u32_e32 v6, s21, v3
	v_lshrrev_b32_e32 v7, 2, v6
	v_lshl_or_b32 v7, v7, 3, v4
	v_and_b32_e32 v8, 3, v6
	v_lshl_or_b32 v8, v8, 6, v5
	v_and_b32_e32 v9, 0xfffffff3, v7
	v_bfe_u32 v10, v7, 2, 1
	v_lshl_or_b32 v9, v10, 3, v9
	v_bfe_u32 v10, v7, 3, 1
	v_lshl_or_b32 v9, v10, 2, v9
	v_lshl_or_b32 v206, v9, 8, v8
	s_add_i32 s21, s15, 8
	s_lshl_b32 s21, s21, 1
	v_add_u32_e32 v6, s21, v3
	v_lshrrev_b32_e32 v7, 2, v6
	v_lshl_or_b32 v7, v7, 3, v4
	v_and_b32_e32 v8, 3, v6
	v_lshl_or_b32 v8, v8, 6, v5
	v_and_b32_e32 v9, 0xfffffff3, v7
	v_bfe_u32 v10, v7, 2, 1
	v_lshl_or_b32 v9, v10, 3, v9
	v_bfe_u32 v10, v7, 3, 1
	v_lshl_or_b32 v9, v10, 2, v9
	v_lshl_or_b32 v207, v9, 8, v8
	v_lshlrev_b32_e32 v4, 2, v3
	v_sub_u32_e32 v252, v2, v4
	s_lshl_b32 s21, s15, 8
	s_add_i32 s21, s21, 0x18000
	v_mov_b32_e32 v253, s21
	s_waitcnt lgkmcnt(0)
	s_mov_b32 s2, s94
.Lfa_task:
	s_cmpk_lt_u32 s2, 0x100
	s_cbranch_scc0 .Lfa_done
	s_and_b32 s21, s2, 7
	s_lshr_b32 s74, s2, 3
	s_lshr_b32 s10, s74, 3
	s_lshl_b32 s21, s21, 2
	s_add_i32 s10, s10, s21
	s_and_b32 s74, s74, 7
	s_lshl_b32 s92, s74, 1
	s_mov_b32 s9, 0
.Lfa_block:
	s_lshr_b32 s21, s9, 1
	s_add_i32 s8, s92, s21
	s_sub_i32 s21, 31, s8
	s_bitcmp1_b32 s9, 0
	s_cselect_b32 s8, s21, s8
	s_lshl_b32 s21, s10, 21
	s_add_u32 s28, s0, 0x402ac000
	s_addc_u32 s29, s1, 0
	s_add_u32 s28, s28, s21
	s_addc_u32 s29, s29, 0
	s_lshr_b32 s74, s10, 1
	s_lshl_b32 s74, s74, 22
	s_add_u32 s34, s0, 0x442ac000
	s_addc_u32 s35, s1, 0
	s_add_u32 s34, s34, s74
	s_addc_u32 s35, s35, 0
	s_add_u32 s38, s34, 0x200000
	s_addc_u32 s39, s35, 0
	s_lshl_b32 s74, s8, 16
	s_add_u32 s40, s0, 0x482ac000
	s_addc_u32 s41, s1, 0
	s_add_u32 s40, s40, s21
	s_addc_u32 s41, s41, 0
	s_add_u32 s40, s40, s74
	s_addc_u32 s41, s41, 0
	s_lshl_b32 s21, s10, 22
	s_add_u32 s42, s0, 0x382ac000
	s_addc_u32 s43, s1, 0
	s_add_u32 s42, s42, s21
	s_addc_u32 s43, s43, 0
	s_add_u32 s42, s42, s74
	s_addc_u32 s43, s43, 0
	s_add_u32 s44, s42, 0x200000
	s_addc_u32 s45, s43, 0
	v_mbcnt_lo_u32_b32 v0, -1, 0
	v_mbcnt_hi_u32_b32 v0, -1, v0
	v_and_b32_e32 v2, 31, v0
	v_lshrrev_b32_e32 v3, 5, v0
	s_lshl_b32 s21, s15, 5
	v_add_u32_e32 v2, s21, v2
	v_lshlrev_b32_e32 v2, 8, v2
	v_lshl_or_b32 v2, v3, 4, v2
	global_load_dwordx4 v[162:165], v2, s[40:41] offset:0
	global_load_dwordx4 v[166:169], v2, s[40:41] offset:32
	global_load_dwordx4 v[170:173], v2, s[40:41] offset:64
	global_load_dwordx4 v[174:177], v2, s[40:41] offset:96
	global_load_dwordx4 v[178:181], v2, s[40:41] offset:128
	global_load_dwordx4 v[182:185], v2, s[40:41] offset:160
	global_load_dwordx4 v[186:189], v2, s[40:41] offset:192
	global_load_dwordx4 v[190:193], v2, s[40:41] offset:224
	v_mov_b32_e32 v0, 0
	v_mov_b32_e32 v1, 0
	v_mov_b32_e32 v3, 0
	v_mov_b32_e32 v4, 0
	v_mov_b32_e32 v5, 0
	v_mov_b32_e32 v6, 0
	v_mov_b32_e32 v7, 0
	v_mov_b32_e32 v8, 0
	v_mov_b32_e32 v9, 0
	v_mov_b32_e32 v10, 0
	v_mov_b32_e32 v11, 0
	v_mov_b32_e32 v12, 0
	v_mov_b32_e32 v13, 0
	v_mov_b32_e32 v14, 0
	v_mov_b32_e32 v15, 0
	v_mov_b32_e32 v16, 0
	v_mov_b32_e32 v17, 0
	v_mov_b32_e32 v18, 0
	v_mov_b32_e32 v19, 0
	v_mov_b32_e32 v20, 0
	v_mov_b32_e32 v21, 0
	v_mov_b32_e32 v22, 0
	v_mov_b32_e32 v23, 0
	v_mov_b32_e32 v24, 0
	v_mov_b32_e32 v25, 0
	v_mov_b32_e32 v26, 0
	v_mov_b32_e32 v27, 0
	v_mov_b32_e32 v28, 0
	v_mov_b32_e32 v29, 0
	v_mov_b32_e32 v30, 0
	v_mov_b32_e32 v31, 0
	v_mov_b32_e32 v32, 0
	v_mov_b32_e32 v33, 0
	v_mov_b32_e32 v34, 0
	v_mov_b32_e32 v35, 0
	v_mov_b32_e32 v36, 0
	v_mov_b32_e32 v37, 0
	v_mov_b32_e32 v38, 0
	v_mov_b32_e32 v39, 0
	v_mov_b32_e32 v40, 0
	v_mov_b32_e32 v41, 0
	v_mov_b32_e32 v42, 0
	v_mov_b32_e32 v43, 0
	v_mov_b32_e32 v44, 0
	v_mov_b32_e32 v45, 0
	v_mov_b32_e32 v46, 0
	v_mov_b32_e32 v47, 0
	v_mov_b32_e32 v48, 0
	v_mov_b32_e32 v49, 0
	v_mov_b32_e32 v50, 0
	v_mov_b32_e32 v51, 0
	v_mov_b32_e32 v52, 0
	v_mov_b32_e32 v53, 0
	v_mov_b32_e32 v54, 0
	v_mov_b32_e32 v55, 0
	v_mov_b32_e32 v56, 0
	v_mov_b32_e32 v57, 0
	v_mov_b32_e32 v58, 0
	v_mov_b32_e32 v59, 0
	v_mov_b32_e32 v60, 0
	v_mov_b32_e32 v61, 0
	v_mov_b32_e32 v62, 0
	v_mov_b32_e32 v63, 0
	v_mov_b32_e32 v64, 0
	v_mov_b32_e32 v65, 0
	v_mov_b32_e32 v66, 0
	v_mov_b32_e32 v67, 0
	v_mov_b32_e32 v68, 0
	v_mov_b32_e32 v69, 0
	v_mov_b32_e32 v70, 0
	v_mov_b32_e32 v71, 0
	v_mov_b32_e32 v72, 0
	v_mov_b32_e32 v73, 0
	v_mov_b32_e32 v74, 0
	v_mov_b32_e32 v75, 0
	v_mov_b32_e32 v76, 0
	v_mov_b32_e32 v77, 0
	v_mov_b32_e32 v78, 0
	v_mov_b32_e32 v79, 0
	v_mov_b32_e32 v80, 0
	v_mov_b32_e32 v81, 0
	v_mov_b32_e32 v82, 0
	v_mov_b32_e32 v83, 0
	v_mov_b32_e32 v84, 0
	v_mov_b32_e32 v85, 0
	v_mov_b32_e32 v86, 0
	v_mov_b32_e32 v87, 0
	v_mov_b32_e32 v88, 0
	v_mov_b32_e32 v89, 0
	v_mov_b32_e32 v90, 0
	v_mov_b32_e32 v91, 0
	v_mov_b32_e32 v92, 0
	v_mov_b32_e32 v93, 0
	v_mov_b32_e32 v94, 0
	v_mov_b32_e32 v95, 0
	v_mov_b32_e32 v98, 0
	v_mov_b32_e32 v99, 0
	v_mov_b32_e32 v100, 0
	v_mov_b32_e32 v101, 0
	v_mov_b32_e32 v102, 0
	v_mov_b32_e32 v103, 0
	v_mov_b32_e32 v104, 0
	v_mov_b32_e32 v105, 0
	v_mov_b32_e32 v106, 0
	v_mov_b32_e32 v107, 0
	v_mov_b32_e32 v108, 0
	v_mov_b32_e32 v109, 0
	v_mov_b32_e32 v110, 0
	v_mov_b32_e32 v111, 0
	v_mov_b32_e32 v112, 0
	v_mov_b32_e32 v113, 0
	v_mov_b32_e32 v114, 0
	v_mov_b32_e32 v115, 0
	v_mov_b32_e32 v116, 0
	v_mov_b32_e32 v117, 0
	v_mov_b32_e32 v118, 0
	v_mov_b32_e32 v119, 0
	v_mov_b32_e32 v120, 0
	v_mov_b32_e32 v121, 0
	v_mov_b32_e32 v122, 0
	v_mov_b32_e32 v123, 0
	v_mov_b32_e32 v124, 0
	v_mov_b32_e32 v125, 0
	v_mov_b32_e32 v126, 0
	v_mov_b32_e32 v127, 0
	v_mov_b32_e32 v128, 0
	v_mov_b32_e32 v129, 0
	v_mov_b32_e32 v2, 0
	v_mov_b32_e32 v96, 0xf149f2ca
	v_mov_b32_e32 v202, 0
	s_add_i32 s5, s8, 1
	s_lshl_b32 s5, s5, 2
	s_lshl_b32 s14, s8, 2
	s_lshr_b32 s21, s15, 1
	s_add_i32 s14, s14, s21
	s_lshl_b32 s24, s8, 8
	s_lshl_b32 s21, s15, 5
	s_add_i32 s24, s24, s21
	s_mov_b32 s4, 0
	s_mov_b32 s64, 0x0
	s_mov_b32 s65, 0x8000
	s_add_i32 s21, s64, s20
	s_mov_b32 m0, s21
	s_nop 0
	global_load_lds_dwordx4 v203, s[28:29]
	s_add_i32 m0, s21, 0x2000
	s_nop 0
	global_load_lds_dwordx4 v204, s[28:29]
	s_add_i32 s21, s65, s20
	s_mov_b32 m0, s21
	s_nop 0
	global_load_lds_dwordx4 v206, s[34:35]
	s_add_i32 m0, s21, 0x2000
	s_nop 0
	global_load_lds_dwordx4 v207, s[34:35]
	s_add_i32 m0, s21, 0x4000
	s_nop 0
	global_load_lds_dwordx4 v206, s[38:39]
	s_add_i32 m0, s21, 0x6000
	s_nop 0
	global_load_lds_dwordx4 v207, s[38:39]
	s_add_u32 s28, s28, 0x4000
	s_addc_u32 s29, s29, 0
	s_add_u32 s34, s34, 0x4000
	s_addc_u32 s35, s35, 0
	s_add_u32 s38, s38, 0x4000
	s_addc_u32 s39, s39, 0
.Lfa_tile:
	s_waitcnt vmcnt(0)
	s_barrier
	s_add_i32 s21, s4, 1
	s_cmp_lt_u32 s21, s5
	s_cbranch_scc0 .Lfa_nodma
	s_and_b32 s64, s21, 1
	s_lshl_b32 s65, s64, 15
	s_lshl_b32 s64, s64, 14
	s_add_i32 s65, s65, 0x8000
	s_add_i32 s21, s64, s20
	s_mov_b32 m0, s21
	s_nop 0
	global_load_lds_dwordx4 v203, s[28:29]
	s_add_i32 m0, s21, 0x2000
	s_nop 0
	global_load_lds_dwordx4 v204, s[28:29]
	s_add_i32 s21, s65, s20
	s_mov_b32 m0, s21
	s_nop 0
	global_load_lds_dwordx4 v206, s[34:35]
	s_add_i32 m0, s21, 0x2000
	s_nop 0
	global_load_lds_dwordx4 v207, s[34:35]
	s_add_i32 m0, s21, 0x4000
	s_nop 0
	global_load_lds_dwordx4 v206, s[38:39]
	s_add_i32 m0, s21, 0x6000
	s_nop 0
	global_load_lds_dwordx4 v207, s[38:39]
	s_add_u32 s28, s28, 0x4000
	s_addc_u32 s29, s29, 0
	s_add_u32 s34, s34, 0x4000
	s_addc_u32 s35, s35, 0
	s_add_u32 s38, s38, 0x4000
	s_addc_u32 s39, s39, 0
.Lfa_nodma:
	s_and_b32 s83, s4, 1
	s_lshl_b32 s84, s83, 15
	s_lshl_b32 s83, s83, 14
	s_add_i32 s84, s84, 0x8000
	v_add_u32_e32 v216, s83, v208
	s_movk_i32 s82, 0
	v_xad_u32 v212, v209, s82, v216
	s_movk_i32 s82, 32
	v_xad_u32 v213, v209, s82, v216
	s_movk_i32 s82, 64
	v_xad_u32 v214, v209, s82, v216
	s_movk_i32 s82, 96
	v_xad_u32 v215, v209, s82, v216
	ds_read_b128 v[228:231], v212 offset:0
	ds_read_b128 v[232:235], v212 offset:8192
	ds_read_b128 v[236:239], v213 offset:0
	ds_read_b128 v[240:243], v213 offset:8192
	s_waitcnt lgkmcnt(2)
	v_mfma_f32_32x32x16_bf16 v[130:145], v[228:231], v[162:165], 0
	v_mfma_f32_32x32x16_bf16 v[146:161], v[232:235], v[162:165], 0
	ds_read_b128 v[228:231], v214 offset:0
	ds_read_b128 v[232:235], v214 offset:8192
	s_waitcnt lgkmcnt(2)
	v_mfma_f32_32x32x16_bf16 v[130:145], v[236:239], v[166:169], v[130:145]
	v_mfma_f32_32x32x16_bf16 v[146:161], v[240:243], v[166:169], v[146:161]
	ds_read_b128 v[236:239], v215 offset:0
	ds_read_b128 v[240:243], v215 offset:8192
	s_waitcnt lgkmcnt(2)
	v_mfma_f32_32x32x16_bf16 v[130:145], v[228:231], v[170:173], v[130:145]
	v_mfma_f32_32x32x16_bf16 v[146:161], v[232:235], v[170:173], v[146:161]
	ds_read_b128 v[228:231], v212 offset:128
	ds_read_b128 v[232:235], v212 offset:8320
	s_waitcnt lgkmcnt(2)
	v_mfma_f32_32x32x16_bf16 v[130:145], v[236:239], v[174:177], v[130:145]
	v_mfma_f32_32x32x16_bf16 v[146:161], v[240:243], v[174:177], v[146:161]
	ds_read_b128 v[236:239], v213 offset:128
	ds_read_b128 v[240:243], v213 offset:8320
	s_waitcnt lgkmcnt(2)
	v_mfma_f32_32x32x16_bf16 v[130:145], v[228:231], v[178:181], v[130:145]
	v_mfma_f32_32x32x16_bf16 v[146:161], v[232:235], v[178:181], v[146:161]
	ds_read_b128 v[228:231], v214 offset:128
	ds_read_b128 v[232:235], v214 offset:8320
	s_waitcnt lgkmcnt(2)
	v_mfma_f32_32x32x16_bf16 v[130:145], v[236:239], v[182:185], v[130:145]
	v_mfma_f32_32x32x16_bf16 v[146:161], v[240:243], v[182:185], v[146:161]
	ds_read_b128 v[236:239], v215 offset:128
	ds_read_b128 v[240:243], v215 offset:8320
	s_waitcnt lgkmcnt(2)
	v_mfma_f32_32x32x16_bf16 v[130:145], v[228:231], v[186:189], v[130:145]
	v_mfma_f32_32x32x16_bf16 v[146:161], v[232:235], v[186:189], v[146:161]
	s_waitcnt lgkmcnt(0)
	v_mfma_f32_32x32x16_bf16 v[130:145], v[236:239], v[190:193], v[130:145]
	v_mfma_f32_32x32x16_bf16 v[146:161], v[240:243], v[190:193], v[146:161]
	s_nop 7
	s_nop 7
	s_cmp_ge_u32 s4, s14
	s_cbranch_scc0 .Lfa_nomask
	s_lshl_b32 s21, s4, 6
	s_sub_i32 s21, s24, s21
	v_add_u32_e32 v228, s21, v252
	v_mov_b32_e32 v229, 0xff800000
	v_cmp_gt_i32_e64 vcc, 0, v228
	v_cmp_gt_i32_e64 s[48:49], 32, v228
	v_cmp_gt_i32_e64 s[50:51], 1, v228
	v_cmp_gt_i32_e64 s[52:53], 33, v228
	v_cndmask_b32_e64 v130, v130, v229, vcc
	v_cndmask_b32_e64 v146, v146, v229, s[48:49]
	v_cndmask_b32_e64 v131, v131, v229, s[50:51]
	v_cndmask_b32_e64 v147, v147, v229, s[52:53]
	v_cmp_gt_i32_e64 vcc, 2, v228
	v_cmp_gt_i32_e64 s[48:49], 34, v228
	v_cmp_gt_i32_e64 s[50:51], 3, v228
	v_cmp_gt_i32_e64 s[52:53], 35, v228
	v_cndmask_b32_e64 v132, v132, v229, vcc
	v_cndmask_b32_e64 v148, v148, v229, s[48:49]
	v_cndmask_b32_e64 v133, v133, v229, s[50:51]
	v_cndmask_b32_e64 v149, v149, v229, s[52:53]
	v_cmp_gt_i32_e64 vcc, 8, v228
	v_cmp_gt_i32_e64 s[48:49], 40, v228
	v_cmp_gt_i32_e64 s[50:51], 9, v228
	v_cmp_gt_i32_e64 s[52:53], 41, v228
	v_cndmask_b32_e64 v134, v134, v229, vcc
	v_cndmask_b32_e64 v150, v150, v229, s[48:49]
	v_cndmask_b32_e64 v135, v135, v229, s[50:51]
	v_cndmask_b32_e64 v151, v151, v229, s[52:53]
	v_cmp_gt_i32_e64 vcc, 10, v228
	v_cmp_gt_i32_e64 s[48:49], 42, v228
	v_cmp_gt_i32_e64 s[50:51], 11, v228
	v_cmp_gt_i32_e64 s[52:53], 43, v228
	v_cndmask_b32_e64 v136, v136, v229, vcc
	v_cndmask_b32_e64 v152, v152, v229, s[48:49]
	v_cndmask_b32_e64 v137, v137, v229, s[50:51]
	v_cndmask_b32_e64 v153, v153, v229, s[52:53]
	v_cmp_gt_i32_e64 vcc, 16, v228
	v_cmp_gt_i32_e64 s[48:49], 48, v228
	v_cmp_gt_i32_e64 s[50:51], 17, v228
	v_cmp_gt_i32_e64 s[52:53], 49, v228
	v_cndmask_b32_e64 v138, v138, v229, vcc
	v_cndmask_b32_e64 v154, v154, v229, s[48:49]
	v_cndmask_b32_e64 v139, v139, v229, s[50:51]
	v_cndmask_b32_e64 v155, v155, v229, s[52:53]
	v_cmp_gt_i32_e64 vcc, 18, v228
	v_cmp_gt_i32_e64 s[48:49], 50, v228
	v_cmp_gt_i32_e64 s[50:51], 19, v228
	v_cmp_gt_i32_e64 s[52:53], 51, v228
	v_cndmask_b32_e64 v140, v140, v229, vcc
	v_cndmask_b32_e64 v156, v156, v229, s[48:49]
	v_cndmask_b32_e64 v141, v141, v229, s[50:51]
	v_cndmask_b32_e64 v157, v157, v229, s[52:53]
	v_cmp_gt_i32_e64 vcc, 24, v228
	v_cmp_gt_i32_e64 s[48:49], 56, v228
	v_cmp_gt_i32_e64 s[50:51], 25, v228
	v_cmp_gt_i32_e64 s[52:53], 57, v228
	v_cndmask_b32_e64 v142, v142, v229, vcc
	v_cndmask_b32_e64 v158, v158, v229, s[48:49]
	v_cndmask_b32_e64 v143, v143, v229, s[50:51]
	v_cndmask_b32_e64 v159, v159, v229, s[52:53]
	v_cmp_gt_i32_e64 vcc, 26, v228
	v_cmp_gt_i32_e64 s[48:49], 58, v228
	v_cmp_gt_i32_e64 s[50:51], 27, v228
	v_cmp_gt_i32_e64 s[52:53], 59, v228
	v_cndmask_b32_e64 v144, v144, v229, vcc
	v_cndmask_b32_e64 v160, v160, v229, s[48:49]
	v_cndmask_b32_e64 v145, v145, v229, s[50:51]
	v_cndmask_b32_e64 v161, v161, v229, s[52:53]
.Lfa_nomask:
	v_max3_f32 v228, v130, v131, v132
	v_max3_f32 v228, v228, v133, v134
	v_max3_f32 v228, v228, v135, v136
	v_max3_f32 v228, v228, v137, v138
	v_max3_f32 v228, v228, v139, v140
	v_max3_f32 v228, v228, v141, v142
	v_max3_f32 v228, v228, v143, v144
	v_max3_f32 v228, v228, v145, v146
	v_max3_f32 v228, v228, v147, v148
	v_max3_f32 v228, v228, v149, v150
	v_max3_f32 v228, v228, v151, v152
	v_max3_f32 v228, v228, v153, v154
	v_max3_f32 v228, v228, v155, v156
	v_max3_f32 v228, v228, v157, v158
	v_max3_f32 v228, v228, v159, v160
	v_max_f32_e32 v228, v228, v161
	v_mov_b32_e32 v229, v228
	s_nop 1
	v_permlane32_swap_b32_e32 v228, v229
	v_max_f32_e32 v228, v228, v229
	v_sub_f32_e32 v229, v228, v96
	v_mov_b32_e32 v231, 0x42b504f3
	v_cmp_gt_f32_e32 vcc, v229, v231
	s_cbranch_vccz .Lfa_fast
	v_max_f32_e32 v231, v96, v228
	v_sub_f32_e32 v230, v96, v231
	v_mul_f32_e32 v230, 0x3e0293ee, v230
	v_exp_f32_e32 v230, v230
	v_mov_b32_e32 v96, v231
	v_mul_f32_e32 v202, v202, v230
	v_mbcnt_lo_u32_b32 v229, -1, 0
	v_mbcnt_hi_u32_b32 v229, -1, v229
	v_and_b32_e32 v231, 31, v229
	v_lshl_add_u32 v231, v231, 2, v253
	v_lshrrev_b32_e32 v229, 5, v229
	v_lshl_add_u32 v229, v229, 4, v253
	ds_write_b32 v231, v230
	s_waitcnt lgkmcnt(0)
	ds_read_b128 v[236:239], v229 offset:0
	ds_read_b128 v[240:243], v229 offset:32
	ds_read_b128 v[244:247], v229 offset:64
	ds_read_b128 v[248:251], v229 offset:96
	s_waitcnt lgkmcnt(0)
	v_pk_mul_f32 v[0:1], v[0:1], v[236:237]
	v_pk_mul_f32 v[2:3], v[2:3], v[238:239]
	v_pk_mul_f32 v[4:5], v[4:5], v[240:241]
	v_pk_mul_f32 v[6:7], v[6:7], v[242:243]
	v_pk_mul_f32 v[8:9], v[8:9], v[244:245]
	v_pk_mul_f32 v[10:11], v[10:11], v[246:247]
	v_pk_mul_f32 v[12:13], v[12:13], v[248:249]
	v_pk_mul_f32 v[14:15], v[14:15], v[250:251]
	v_pk_mul_f32 v[16:17], v[16:17], v[236:237]
	v_pk_mul_f32 v[18:19], v[18:19], v[238:239]
	v_pk_mul_f32 v[20:21], v[20:21], v[240:241]
	v_pk_mul_f32 v[22:23], v[22:23], v[242:243]
	v_pk_mul_f32 v[24:25], v[24:25], v[244:245]
	v_pk_mul_f32 v[26:27], v[26:27], v[246:247]
	v_pk_mul_f32 v[28:29], v[28:29], v[248:249]
	v_pk_mul_f32 v[30:31], v[30:31], v[250:251]
	v_pk_mul_f32 v[32:33], v[32:33], v[236:237]
	v_pk_mul_f32 v[34:35], v[34:35], v[238:239]
	v_pk_mul_f32 v[36:37], v[36:37], v[240:241]
	v_pk_mul_f32 v[38:39], v[38:39], v[242:243]
	v_pk_mul_f32 v[40:41], v[40:41], v[244:245]
	v_pk_mul_f32 v[42:43], v[42:43], v[246:247]
	v_pk_mul_f32 v[44:45], v[44:45], v[248:249]
	v_pk_mul_f32 v[46:47], v[46:47], v[250:251]
	v_pk_mul_f32 v[48:49], v[48:49], v[236:237]
	v_pk_mul_f32 v[50:51], v[50:51], v[238:239]
	v_pk_mul_f32 v[52:53], v[52:53], v[240:241]
	v_pk_mul_f32 v[54:55], v[54:55], v[242:243]
	v_pk_mul_f32 v[56:57], v[56:57], v[244:245]
	v_pk_mul_f32 v[58:59], v[58:59], v[246:247]
	v_pk_mul_f32 v[60:61], v[60:61], v[248:249]
	v_pk_mul_f32 v[62:63], v[62:63], v[250:251]
	v_pk_mul_f32 v[64:65], v[64:65], v[236:237]
	v_pk_mul_f32 v[66:67], v[66:67], v[238:239]
	v_pk_mul_f32 v[68:69], v[68:69], v[240:241]
	v_pk_mul_f32 v[70:71], v[70:71], v[242:243]
	v_pk_mul_f32 v[72:73], v[72:73], v[244:245]
	v_pk_mul_f32 v[74:75], v[74:75], v[246:247]
	v_pk_mul_f32 v[76:77], v[76:77], v[248:249]
	v_pk_mul_f32 v[78:79], v[78:79], v[250:251]
	v_pk_mul_f32 v[80:81], v[80:81], v[236:237]
	v_pk_mul_f32 v[82:83], v[82:83], v[238:239]
	v_pk_mul_f32 v[84:85], v[84:85], v[240:241]
	v_pk_mul_f32 v[86:87], v[86:87], v[242:243]
	v_pk_mul_f32 v[88:89], v[88:89], v[244:245]
	v_pk_mul_f32 v[90:91], v[90:91], v[246:247]
	v_pk_mul_f32 v[92:93], v[92:93], v[248:249]
	v_pk_mul_f32 v[94:95], v[94:95], v[250:251]
	v_pk_mul_f32 v[98:99], v[98:99], v[236:237]
	v_pk_mul_f32 v[100:101], v[100:101], v[238:239]
	v_pk_mul_f32 v[102:103], v[102:103], v[240:241]
	v_pk_mul_f32 v[104:105], v[104:105], v[242:243]
	v_pk_mul_f32 v[106:107], v[106:107], v[244:245]
	v_pk_mul_f32 v[108:109], v[108:109], v[246:247]
	v_pk_mul_f32 v[110:111], v[110:111], v[248:249]
	v_pk_mul_f32 v[112:113], v[112:113], v[250:251]
	v_pk_mul_f32 v[114:115], v[114:115], v[236:237]
	v_pk_mul_f32 v[116:117], v[116:117], v[238:239]
	v_pk_mul_f32 v[118:119], v[118:119], v[240:241]
	v_pk_mul_f32 v[120:121], v[120:121], v[242:243]
	v_pk_mul_f32 v[122:123], v[122:123], v[244:245]
	v_pk_mul_f32 v[124:125], v[124:125], v[246:247]
	v_pk_mul_f32 v[126:127], v[126:127], v[248:249]
	v_pk_mul_f32 v[128:129], v[128:129], v[250:251]
.Lfa_fast:
	v_mul_f32_e32 v231, 0xbe0293ee, v96
	v_mov_b32_e32 v229, 0x3e0293ee
	v_fma_f32 v130, v130, v229, v231
	v_fma_f32 v131, v131, v229, v231
	v_fma_f32 v132, v132, v229, v231
	v_fma_f32 v133, v133, v229, v231
	v_fma_f32 v134, v134, v229, v231
	v_fma_f32 v135, v135, v229, v231
	v_fma_f32 v136, v136, v229, v231
	v_fma_f32 v137, v137, v229, v231
	v_fma_f32 v138, v138, v229, v231
	v_fma_f32 v139, v139, v229, v231
	v_fma_f32 v140, v140, v229, v231
	v_fma_f32 v141, v141, v229, v231
	v_fma_f32 v142, v142, v229, v231
	v_fma_f32 v143, v143, v229, v231
	v_fma_f32 v144, v144, v229, v231
	v_fma_f32 v145, v145, v229, v231
	v_fma_f32 v146, v146, v229, v231
	v_fma_f32 v147, v147, v229, v231
	v_fma_f32 v148, v148, v229, v231
	v_fma_f32 v149, v149, v229, v231
	v_fma_f32 v150, v150, v229, v231
	v_fma_f32 v151, v151, v229, v231
	v_fma_f32 v152, v152, v229, v231
	v_fma_f32 v153, v153, v229, v231
	v_fma_f32 v154, v154, v229, v231
	v_fma_f32 v155, v155, v229, v231
	v_fma_f32 v156, v156, v229, v231
	v_fma_f32 v157, v157, v229, v231
	v_fma_f32 v158, v158, v229, v231
	v_fma_f32 v159, v159, v229, v231
	v_fma_f32 v160, v160, v229, v231
	v_fma_f32 v161, v161, v229, v231
	v_exp_f32_e32 v130, v130
	v_exp_f32_e32 v131, v131
	v_exp_f32_e32 v132, v132
	v_exp_f32_e32 v133, v133
	v_exp_f32_e32 v134, v134
	v_exp_f32_e32 v135, v135
	v_exp_f32_e32 v136, v136
	v_exp_f32_e32 v137, v137
	v_exp_f32_e32 v138, v138
	v_exp_f32_e32 v139, v139
	v_exp_f32_e32 v140, v140
	v_exp_f32_e32 v141, v141
	v_exp_f32_e32 v142, v142
	v_exp_f32_e32 v143, v143
	v_exp_f32_e32 v144, v144
	v_exp_f32_e32 v145, v145
	v_exp_f32_e32 v146, v146
	v_exp_f32_e32 v147, v147
	v_exp_f32_e32 v148, v148
	v_exp_f32_e32 v149, v149
	v_exp_f32_e32 v150, v150
	v_exp_f32_e32 v151, v151
	v_exp_f32_e32 v152, v152
	v_exp_f32_e32 v153, v153
	v_exp_f32_e32 v154, v154
	v_exp_f32_e32 v155, v155
	v_exp_f32_e32 v156, v156
	v_exp_f32_e32 v157, v157
	v_exp_f32_e32 v158, v158
	v_exp_f32_e32 v159, v159
	v_exp_f32_e32 v160, v160
	v_exp_f32_e32 v161, v161
	s_nop 0
	v_add_f32_e32 v232, v130, v131
	v_add_f32_e32 v232, v232, v132
	v_add_f32_e32 v232, v232, v133
	v_add_f32_e32 v232, v232, v134
	v_add_f32_e32 v232, v232, v135
	v_add_f32_e32 v232, v232, v136
	v_add_f32_e32 v232, v232, v137
	v_add_f32_e32 v232, v232, v138
	v_add_f32_e32 v232, v232, v139
	v_add_f32_e32 v232, v232, v140
	v_add_f32_e32 v232, v232, v141
	v_add_f32_e32 v232, v232, v142
	v_add_f32_e32 v232, v232, v143
	v_add_f32_e32 v232, v232, v144
	v_add_f32_e32 v232, v232, v145
	v_add_f32_e32 v232, v232, v146
	v_add_f32_e32 v232, v232, v147
	v_add_f32_e32 v232, v232, v148
	v_add_f32_e32 v232, v232, v149
	v_add_f32_e32 v232, v232, v150
	v_add_f32_e32 v232, v232, v151
	v_add_f32_e32 v232, v232, v152
	v_add_f32_e32 v232, v232, v153
	v_add_f32_e32 v232, v232, v154
	v_add_f32_e32 v232, v232, v155
	v_add_f32_e32 v232, v232, v156
	v_add_f32_e32 v232, v232, v157
	v_add_f32_e32 v232, v232, v158
	v_add_f32_e32 v232, v232, v159
	v_add_f32_e32 v232, v232, v160
	v_add_f32_e32 v232, v232, v161
	v_mov_b32_e32 v229, v232
	s_nop 1
	v_permlane32_swap_b32_e32 v232, v229
	v_add_f32_e32 v232, v232, v229
	v_add_f32_e32 v202, v202, v232
	v_cvt_pk_bf16_f32 v212, v130, v131
	v_cvt_pk_bf16_f32 v213, v132, v133
	v_cvt_pk_bf16_f32 v214, v134, v135
	v_cvt_pk_bf16_f32 v215, v136, v137
	v_cvt_pk_bf16_f32 v216, v138, v139
	v_cvt_pk_bf16_f32 v217, v140, v141
	v_cvt_pk_bf16_f32 v218, v142, v143
	v_cvt_pk_bf16_f32 v219, v144, v145
	v_cvt_pk_bf16_f32 v220, v146, v147
	v_cvt_pk_bf16_f32 v221, v148, v149
	v_cvt_pk_bf16_f32 v222, v150, v151
	v_cvt_pk_bf16_f32 v223, v152, v153
	v_cvt_pk_bf16_f32 v224, v154, v155
	v_cvt_pk_bf16_f32 v225, v156, v157
	v_cvt_pk_bf16_f32 v226, v158, v159
	v_cvt_pk_bf16_f32 v227, v160, v161
	s_nop 1
	v_permlane32_swap_b32_e32 v212, v214
	v_permlane32_swap_b32_e32 v213, v215
	v_permlane32_swap_b32_e32 v216, v218
	v_permlane32_swap_b32_e32 v217, v219
	v_permlane32_swap_b32_e32 v220, v222
	v_permlane32_swap_b32_e32 v221, v223
	v_permlane32_swap_b32_e32 v224, v226
	v_permlane32_swap_b32_e32 v225, v227
	v_add_u32_e32 v130, s84, v210
	ds_read_b64_tr_b16 v[228:229], v130 offset:0
	ds_read_b64_tr_b16 v[230:231], v130 offset:2048
	ds_read_b64_tr_b16 v[232:233], v130 offset:4096
	ds_read_b64_tr_b16 v[234:235], v130 offset:6144
	ds_read_b64_tr_b16 v[236:237], v130 offset:8192
	ds_read_b64_tr_b16 v[238:239], v130 offset:10240
	ds_read_b64_tr_b16 v[240:241], v130 offset:12288
	ds_read_b64_tr_b16 v[242:243], v130 offset:14336
	ds_read_b64_tr_b16 v[244:245], v130 offset:512
	ds_read_b64_tr_b16 v[246:247], v130 offset:2560
	ds_read_b64_tr_b16 v[248:249], v130 offset:4608
	ds_read_b64_tr_b16 v[250:251], v130 offset:6656
	ds_read_b64_tr_b16 v[194:195], v130 offset:8704
	ds_read_b64_tr_b16 v[196:197], v130 offset:10752
	ds_read_b64_tr_b16 v[198:199], v130 offset:12800
	ds_read_b64_tr_b16 v[200:201], v130 offset:14848
	s_waitcnt lgkmcnt(8)
	v_mfma_f32_32x32x16_bf16 v[0:15], v[212:215], v[228:231], v[0:15]
	v_mfma_f32_32x32x16_bf16 v[0:15], v[216:219], v[232:235], v[0:15]
	v_mfma_f32_32x32x16_bf16 v[0:15], v[220:223], v[236:239], v[0:15]
	v_mfma_f32_32x32x16_bf16 v[0:15], v[224:227], v[240:243], v[0:15]
	ds_read_b64_tr_b16 v[228:229], v130 offset:1024
	ds_read_b64_tr_b16 v[230:231], v130 offset:3072
	ds_read_b64_tr_b16 v[232:233], v130 offset:5120
	ds_read_b64_tr_b16 v[234:235], v130 offset:7168
	ds_read_b64_tr_b16 v[236:237], v130 offset:9216
	ds_read_b64_tr_b16 v[238:239], v130 offset:11264
	ds_read_b64_tr_b16 v[240:241], v130 offset:13312
	ds_read_b64_tr_b16 v[242:243], v130 offset:15360
	s_waitcnt lgkmcnt(8)
	v_mfma_f32_32x32x16_bf16 v[16:31], v[212:215], v[244:247], v[16:31]
	v_mfma_f32_32x32x16_bf16 v[16:31], v[216:219], v[248:251], v[16:31]
	v_mfma_f32_32x32x16_bf16 v[16:31], v[220:223], v[194:197], v[16:31]
	v_mfma_f32_32x32x16_bf16 v[16:31], v[224:227], v[198:201], v[16:31]
	ds_read_b64_tr_b16 v[244:245], v130 offset:1536
	ds_read_b64_tr_b16 v[246:247], v130 offset:3584
	ds_read_b64_tr_b16 v[248:249], v130 offset:5632
	ds_read_b64_tr_b16 v[250:251], v130 offset:7680
	ds_read_b64_tr_b16 v[194:195], v130 offset:9728
	ds_read_b64_tr_b16 v[196:197], v130 offset:11776
	ds_read_b64_tr_b16 v[198:199], v130 offset:13824
	ds_read_b64_tr_b16 v[200:201], v130 offset:15872
	s_waitcnt lgkmcnt(8)
	v_mfma_f32_32x32x16_bf16 v[32:47], v[212:215], v[228:231], v[32:47]
	v_mfma_f32_32x32x16_bf16 v[32:47], v[216:219], v[232:235], v[32:47]
	v_mfma_f32_32x32x16_bf16 v[32:47], v[220:223], v[236:239], v[32:47]
	v_mfma_f32_32x32x16_bf16 v[32:47], v[224:227], v[240:243], v[32:47]
	ds_read_b64_tr_b16 v[228:229], v130 offset:16384
	ds_read_b64_tr_b16 v[230:231], v130 offset:18432
	ds_read_b64_tr_b16 v[232:233], v130 offset:20480
	ds_read_b64_tr_b16 v[234:235], v130 offset:22528
	ds_read_b64_tr_b16 v[236:237], v130 offset:24576
	ds_read_b64_tr_b16 v[238:239], v130 offset:26624
	ds_read_b64_tr_b16 v[240:241], v130 offset:28672
	ds_read_b64_tr_b16 v[242:243], v130 offset:30720
	s_waitcnt lgkmcnt(8)
	v_mfma_f32_32x32x16_bf16 v[48:63], v[212:215], v[244:247], v[48:63]
	v_mfma_f32_32x32x16_bf16 v[48:63], v[216:219], v[248:251], v[48:63]
	v_mfma_f32_32x32x16_bf16 v[48:63], v[220:223], v[194:197], v[48:63]
	v_mfma_f32_32x32x16_bf16 v[48:63], v[224:227], v[198:201], v[48:63]
	ds_read_b64_tr_b16 v[244:245], v130 offset:16896
	ds_read_b64_tr_b16 v[246:247], v130 offset:18944
	ds_read_b64_tr_b16 v[248:249], v130 offset:20992
	ds_read_b64_tr_b16 v[250:251], v130 offset:23040
	ds_read_b64_tr_b16 v[194:195], v130 offset:25088
	ds_read_b64_tr_b16 v[196:197], v130 offset:27136
	ds_read_b64_tr_b16 v[198:199], v130 offset:29184
	ds_read_b64_tr_b16 v[200:201], v130 offset:31232
	s_waitcnt lgkmcnt(8)
	v_mfma_f32_32x32x16_bf16 v[64:79], v[212:215], v[228:231], v[64:79]
	v_mfma_f32_32x32x16_bf16 v[64:79], v[216:219], v[232:235], v[64:79]
	v_mfma_f32_32x32x16_bf16 v[64:79], v[220:223], v[236:239], v[64:79]
	v_mfma_f32_32x32x16_bf16 v[64:79], v[224:227], v[240:243], v[64:79]
	ds_read_b64_tr_b16 v[228:229], v130 offset:17408
	ds_read_b64_tr_b16 v[230:231], v130 offset:19456
	ds_read_b64_tr_b16 v[232:233], v130 offset:21504
	ds_read_b64_tr_b16 v[234:235], v130 offset:23552
	ds_read_b64_tr_b16 v[236:237], v130 offset:25600
	ds_read_b64_tr_b16 v[238:239], v130 offset:27648
	ds_read_b64_tr_b16 v[240:241], v130 offset:29696
	ds_read_b64_tr_b16 v[242:243], v130 offset:31744
	s_waitcnt lgkmcnt(8)
	v_mfma_f32_32x32x16_bf16 v[80:95], v[212:215], v[244:247], v[80:95]
	v_mfma_f32_32x32x16_bf16 v[80:95], v[216:219], v[248:251], v[80:95]
	v_mfma_f32_32x32x16_bf16 v[80:95], v[220:223], v[194:197], v[80:95]
	v_mfma_f32_32x32x16_bf16 v[80:95], v[224:227], v[198:201], v[80:95]
	ds_read_b64_tr_b16 v[244:245], v130 offset:17920
	ds_read_b64_tr_b16 v[246:247], v130 offset:19968
	ds_read_b64_tr_b16 v[248:249], v130 offset:22016
	ds_read_b64_tr_b16 v[250:251], v130 offset:24064
	ds_read_b64_tr_b16 v[194:195], v130 offset:26112
	ds_read_b64_tr_b16 v[196:197], v130 offset:28160
	ds_read_b64_tr_b16 v[198:199], v130 offset:30208
	ds_read_b64_tr_b16 v[200:201], v130 offset:32256
	s_waitcnt lgkmcnt(8)
	v_mfma_f32_32x32x16_bf16 v[98:113], v[212:215], v[228:231], v[98:113]
	v_mfma_f32_32x32x16_bf16 v[98:113], v[216:219], v[232:235], v[98:113]
	v_mfma_f32_32x32x16_bf16 v[98:113], v[220:223], v[236:239], v[98:113]
	v_mfma_f32_32x32x16_bf16 v[98:113], v[224:227], v[240:243], v[98:113]
	s_waitcnt lgkmcnt(0)
	v_mfma_f32_32x32x16_bf16 v[114:129], v[212:215], v[244:247], v[114:129]
	v_mfma_f32_32x32x16_bf16 v[114:129], v[216:219], v[248:251], v[114:129]
	v_mfma_f32_32x32x16_bf16 v[114:129], v[220:223], v[194:197], v[114:129]
	v_mfma_f32_32x32x16_bf16 v[114:129], v[224:227], v[198:201], v[114:129]
	s_add_i32 s4, s4, 1
	s_cmp_lt_u32 s4, s5
	s_cbranch_scc1 .Lfa_tile
	s_nop 7
	s_nop 7
	v_mbcnt_lo_u32_b32 v229, -1, 0
	v_mbcnt_hi_u32_b32 v229, -1, v229
	v_and_b32_e32 v231, 31, v229
	v_lshl_add_u32 v230, v231, 2, v253
	v_lshrrev_b32_e32 v229, 5, v229
	v_lshl_add_u32 v232, v229, 4, v253
	ds_write_b32 v230, v202 offset:128
	s_waitcnt lgkmcnt(0)
	ds_read_b128 v[236:239], v232 offset:128
	ds_read_b128 v[240:243], v232 offset:160
	ds_read_b128 v[244:247], v232 offset:192
	ds_read_b128 v[248:251], v232 offset:224
	s_lshl_b32 s21, s15, 13
	v_lshlrev_b32_e32 v233, 10, v229
	v_lshl_add_u32 v233, v231, 1, v233
	v_add_u32_e32 v233, s21, v233
	v_add_u32_e32 v234, 0x1000, v233
	s_waitcnt lgkmcnt(0)
	v_rcp_f32_e32 v236, v236
	v_rcp_f32_e32 v237, v237
	v_rcp_f32_e32 v238, v238
	v_rcp_f32_e32 v239, v239
	v_rcp_f32_e32 v240, v240
	v_rcp_f32_e32 v241, v241
	v_rcp_f32_e32 v242, v242
	v_rcp_f32_e32 v243, v243
	v_rcp_f32_e32 v244, v244
	v_rcp_f32_e32 v245, v245
	v_rcp_f32_e32 v246, v246
	v_rcp_f32_e32 v247, v247
	v_rcp_f32_e32 v248, v248
	v_rcp_f32_e32 v249, v249
	v_rcp_f32_e32 v250, v250
	v_rcp_f32_e32 v251, v251
	s_nop 0
	v_mul_f32_dpp v228, v0, v236 quad_perm:[1,0,3,2] row_mask:0xf bank_mask:0xf
	v_mul_f32_e32 v0, v0, v236
	v_cvt_pk_bf16_f32 v0, v0, v228
	v_mul_f32_dpp v228, v1, v237 quad_perm:[1,0,3,2] row_mask:0xf bank_mask:0xf
	v_mul_f32_e32 v1, v1, v237
	v_cvt_pk_bf16_f32 v1, v1, v228
	v_mul_f32_dpp v228, v2, v238 quad_perm:[1,0,3,2] row_mask:0xf bank_mask:0xf
	v_mul_f32_e32 v2, v2, v238
	v_cvt_pk_bf16_f32 v2, v2, v228
	v_mul_f32_dpp v228, v3, v239 quad_perm:[1,0,3,2] row_mask:0xf bank_mask:0xf
	v_mul_f32_e32 v3, v3, v239
	v_cvt_pk_bf16_f32 v3, v3, v228
	v_mul_f32_dpp v228, v4, v240 quad_perm:[1,0,3,2] row_mask:0xf bank_mask:0xf
	v_mul_f32_e32 v4, v4, v240
	v_cvt_pk_bf16_f32 v4, v4, v228
	v_mul_f32_dpp v228, v5, v241 quad_perm:[1,0,3,2] row_mask:0xf bank_mask:0xf
	v_mul_f32_e32 v5, v5, v241
	v_cvt_pk_bf16_f32 v5, v5, v228
	v_mul_f32_dpp v228, v6, v242 quad_perm:[1,0,3,2] row_mask:0xf bank_mask:0xf
	v_mul_f32_e32 v6, v6, v242
	v_cvt_pk_bf16_f32 v6, v6, v228
	v_mul_f32_dpp v228, v7, v243 quad_perm:[1,0,3,2] row_mask:0xf bank_mask:0xf
	v_mul_f32_e32 v7, v7, v243
	v_cvt_pk_bf16_f32 v7, v7, v228
	v_mul_f32_dpp v228, v8, v244 quad_perm:[1,0,3,2] row_mask:0xf bank_mask:0xf
	v_mul_f32_e32 v8, v8, v244
	v_cvt_pk_bf16_f32 v8, v8, v228
	v_mul_f32_dpp v228, v9, v245 quad_perm:[1,0,3,2] row_mask:0xf bank_mask:0xf
	v_mul_f32_e32 v9, v9, v245
	v_cvt_pk_bf16_f32 v9, v9, v228
	v_mul_f32_dpp v228, v10, v246 quad_perm:[1,0,3,2] row_mask:0xf bank_mask:0xf
	v_mul_f32_e32 v10, v10, v246
	v_cvt_pk_bf16_f32 v10, v10, v228
	v_mul_f32_dpp v228, v11, v247 quad_perm:[1,0,3,2] row_mask:0xf bank_mask:0xf
	v_mul_f32_e32 v11, v11, v247
	v_cvt_pk_bf16_f32 v11, v11, v228
	v_mul_f32_dpp v228, v12, v248 quad_perm:[1,0,3,2] row_mask:0xf bank_mask:0xf
	v_mul_f32_e32 v12, v12, v248
	v_cvt_pk_bf16_f32 v12, v12, v228
	v_mul_f32_dpp v228, v13, v249 quad_perm:[1,0,3,2] row_mask:0xf bank_mask:0xf
	v_mul_f32_e32 v13, v13, v249
	v_cvt_pk_bf16_f32 v13, v13, v228
	v_mul_f32_dpp v228, v14, v250 quad_perm:[1,0,3,2] row_mask:0xf bank_mask:0xf
	v_mul_f32_e32 v14, v14, v250
	v_cvt_pk_bf16_f32 v14, v14, v228
	v_mul_f32_dpp v228, v15, v251 quad_perm:[1,0,3,2] row_mask:0xf bank_mask:0xf
	v_mul_f32_e32 v15, v15, v251
	v_cvt_pk_bf16_f32 v15, v15, v228
	v_mul_f32_dpp v228, v16, v236 quad_perm:[1,0,3,2] row_mask:0xf bank_mask:0xf
	v_mul_f32_e32 v16, v16, v236
	v_cvt_pk_bf16_f32 v16, v16, v228
	v_mul_f32_dpp v228, v17, v237 quad_perm:[1,0,3,2] row_mask:0xf bank_mask:0xf
	v_mul_f32_e32 v17, v17, v237
	v_cvt_pk_bf16_f32 v17, v17, v228
	v_mul_f32_dpp v228, v18, v238 quad_perm:[1,0,3,2] row_mask:0xf bank_mask:0xf
	v_mul_f32_e32 v18, v18, v238
	v_cvt_pk_bf16_f32 v18, v18, v228
	v_mul_f32_dpp v228, v19, v239 quad_perm:[1,0,3,2] row_mask:0xf bank_mask:0xf
	v_mul_f32_e32 v19, v19, v239
	v_cvt_pk_bf16_f32 v19, v19, v228
	v_mul_f32_dpp v228, v20, v240 quad_perm:[1,0,3,2] row_mask:0xf bank_mask:0xf
	v_mul_f32_e32 v20, v20, v240
	v_cvt_pk_bf16_f32 v20, v20, v228
	v_mul_f32_dpp v228, v21, v241 quad_perm:[1,0,3,2] row_mask:0xf bank_mask:0xf
	v_mul_f32_e32 v21, v21, v241
	v_cvt_pk_bf16_f32 v21, v21, v228
	v_mul_f32_dpp v228, v22, v242 quad_perm:[1,0,3,2] row_mask:0xf bank_mask:0xf
	v_mul_f32_e32 v22, v22, v242
	v_cvt_pk_bf16_f32 v22, v22, v228
	v_mul_f32_dpp v228, v23, v243 quad_perm:[1,0,3,2] row_mask:0xf bank_mask:0xf
	v_mul_f32_e32 v23, v23, v243
	v_cvt_pk_bf16_f32 v23, v23, v228
	v_mul_f32_dpp v228, v24, v244 quad_perm:[1,0,3,2] row_mask:0xf bank_mask:0xf
	v_mul_f32_e32 v24, v24, v244
	v_cvt_pk_bf16_f32 v24, v24, v228
	v_mul_f32_dpp v228, v25, v245 quad_perm:[1,0,3,2] row_mask:0xf bank_mask:0xf
	v_mul_f32_e32 v25, v25, v245
	v_cvt_pk_bf16_f32 v25, v25, v228
	v_mul_f32_dpp v228, v26, v246 quad_perm:[1,0,3,2] row_mask:0xf bank_mask:0xf
	v_mul_f32_e32 v26, v26, v246
	v_cvt_pk_bf16_f32 v26, v26, v228
	v_mul_f32_dpp v228, v27, v247 quad_perm:[1,0,3,2] row_mask:0xf bank_mask:0xf
	v_mul_f32_e32 v27, v27, v247
	v_cvt_pk_bf16_f32 v27, v27, v228
	v_mul_f32_dpp v228, v28, v248 quad_perm:[1,0,3,2] row_mask:0xf bank_mask:0xf
	v_mul_f32_e32 v28, v28, v248
	v_cvt_pk_bf16_f32 v28, v28, v228
	v_mul_f32_dpp v228, v29, v249 quad_perm:[1,0,3,2] row_mask:0xf bank_mask:0xf
	v_mul_f32_e32 v29, v29, v249
	v_cvt_pk_bf16_f32 v29, v29, v228
	v_mul_f32_dpp v228, v30, v250 quad_perm:[1,0,3,2] row_mask:0xf bank_mask:0xf
	v_mul_f32_e32 v30, v30, v250
	v_cvt_pk_bf16_f32 v30, v30, v228
	v_mul_f32_dpp v228, v31, v251 quad_perm:[1,0,3,2] row_mask:0xf bank_mask:0xf
	v_mul_f32_e32 v31, v31, v251
	v_cvt_pk_bf16_f32 v31, v31, v228
	v_mul_f32_dpp v228, v32, v236 quad_perm:[1,0,3,2] row_mask:0xf bank_mask:0xf
	v_mul_f32_e32 v32, v32, v236
	v_cvt_pk_bf16_f32 v32, v32, v228
	v_mul_f32_dpp v228, v33, v237 quad_perm:[1,0,3,2] row_mask:0xf bank_mask:0xf
	v_mul_f32_e32 v33, v33, v237
	v_cvt_pk_bf16_f32 v33, v33, v228
	v_mul_f32_dpp v228, v34, v238 quad_perm:[1,0,3,2] row_mask:0xf bank_mask:0xf
	v_mul_f32_e32 v34, v34, v238
	v_cvt_pk_bf16_f32 v34, v34, v228
	v_mul_f32_dpp v228, v35, v239 quad_perm:[1,0,3,2] row_mask:0xf bank_mask:0xf
	v_mul_f32_e32 v35, v35, v239
	v_cvt_pk_bf16_f32 v35, v35, v228
	v_mul_f32_dpp v228, v36, v240 quad_perm:[1,0,3,2] row_mask:0xf bank_mask:0xf
	v_mul_f32_e32 v36, v36, v240
	v_cvt_pk_bf16_f32 v36, v36, v228
	v_mul_f32_dpp v228, v37, v241 quad_perm:[1,0,3,2] row_mask:0xf bank_mask:0xf
	v_mul_f32_e32 v37, v37, v241
	v_cvt_pk_bf16_f32 v37, v37, v228
	v_mul_f32_dpp v228, v38, v242 quad_perm:[1,0,3,2] row_mask:0xf bank_mask:0xf
	v_mul_f32_e32 v38, v38, v242
	v_cvt_pk_bf16_f32 v38, v38, v228
	v_mul_f32_dpp v228, v39, v243 quad_perm:[1,0,3,2] row_mask:0xf bank_mask:0xf
	v_mul_f32_e32 v39, v39, v243
	v_cvt_pk_bf16_f32 v39, v39, v228
	v_mul_f32_dpp v228, v40, v244 quad_perm:[1,0,3,2] row_mask:0xf bank_mask:0xf
	v_mul_f32_e32 v40, v40, v244
	v_cvt_pk_bf16_f32 v40, v40, v228
	v_mul_f32_dpp v228, v41, v245 quad_perm:[1,0,3,2] row_mask:0xf bank_mask:0xf
	v_mul_f32_e32 v41, v41, v245
	v_cvt_pk_bf16_f32 v41, v41, v228
	v_mul_f32_dpp v228, v42, v246 quad_perm:[1,0,3,2] row_mask:0xf bank_mask:0xf
	v_mul_f32_e32 v42, v42, v246
	v_cvt_pk_bf16_f32 v42, v42, v228
	v_mul_f32_dpp v228, v43, v247 quad_perm:[1,0,3,2] row_mask:0xf bank_mask:0xf
	v_mul_f32_e32 v43, v43, v247
	v_cvt_pk_bf16_f32 v43, v43, v228
	v_mul_f32_dpp v228, v44, v248 quad_perm:[1,0,3,2] row_mask:0xf bank_mask:0xf
	v_mul_f32_e32 v44, v44, v248
	v_cvt_pk_bf16_f32 v44, v44, v228
	v_mul_f32_dpp v228, v45, v249 quad_perm:[1,0,3,2] row_mask:0xf bank_mask:0xf
	v_mul_f32_e32 v45, v45, v249
	v_cvt_pk_bf16_f32 v45, v45, v228
	v_mul_f32_dpp v228, v46, v250 quad_perm:[1,0,3,2] row_mask:0xf bank_mask:0xf
	v_mul_f32_e32 v46, v46, v250
	v_cvt_pk_bf16_f32 v46, v46, v228
	v_mul_f32_dpp v228, v47, v251 quad_perm:[1,0,3,2] row_mask:0xf bank_mask:0xf
	v_mul_f32_e32 v47, v47, v251
	v_cvt_pk_bf16_f32 v47, v47, v228
	v_mul_f32_dpp v228, v48, v236 quad_perm:[1,0,3,2] row_mask:0xf bank_mask:0xf
	v_mul_f32_e32 v48, v48, v236
	v_cvt_pk_bf16_f32 v48, v48, v228
	v_mul_f32_dpp v228, v49, v237 quad_perm:[1,0,3,2] row_mask:0xf bank_mask:0xf
	v_mul_f32_e32 v49, v49, v237
	v_cvt_pk_bf16_f32 v49, v49, v228
	v_mul_f32_dpp v228, v50, v238 quad_perm:[1,0,3,2] row_mask:0xf bank_mask:0xf
	v_mul_f32_e32 v50, v50, v238
	v_cvt_pk_bf16_f32 v50, v50, v228
	v_mul_f32_dpp v228, v51, v239 quad_perm:[1,0,3,2] row_mask:0xf bank_mask:0xf
	v_mul_f32_e32 v51, v51, v239
	v_cvt_pk_bf16_f32 v51, v51, v228
	v_mul_f32_dpp v228, v52, v240 quad_perm:[1,0,3,2] row_mask:0xf bank_mask:0xf
	v_mul_f32_e32 v52, v52, v240
	v_cvt_pk_bf16_f32 v52, v52, v228
	v_mul_f32_dpp v228, v53, v241 quad_perm:[1,0,3,2] row_mask:0xf bank_mask:0xf
	v_mul_f32_e32 v53, v53, v241
	v_cvt_pk_bf16_f32 v53, v53, v228
	v_mul_f32_dpp v228, v54, v242 quad_perm:[1,0,3,2] row_mask:0xf bank_mask:0xf
	v_mul_f32_e32 v54, v54, v242
	v_cvt_pk_bf16_f32 v54, v54, v228
	v_mul_f32_dpp v228, v55, v243 quad_perm:[1,0,3,2] row_mask:0xf bank_mask:0xf
	v_mul_f32_e32 v55, v55, v243
	v_cvt_pk_bf16_f32 v55, v55, v228
	v_mul_f32_dpp v228, v56, v244 quad_perm:[1,0,3,2] row_mask:0xf bank_mask:0xf
	v_mul_f32_e32 v56, v56, v244
	v_cvt_pk_bf16_f32 v56, v56, v228
	v_mul_f32_dpp v228, v57, v245 quad_perm:[1,0,3,2] row_mask:0xf bank_mask:0xf
	v_mul_f32_e32 v57, v57, v245
	v_cvt_pk_bf16_f32 v57, v57, v228
	v_mul_f32_dpp v228, v58, v246 quad_perm:[1,0,3,2] row_mask:0xf bank_mask:0xf
	v_mul_f32_e32 v58, v58, v246
	v_cvt_pk_bf16_f32 v58, v58, v228
	v_mul_f32_dpp v228, v59, v247 quad_perm:[1,0,3,2] row_mask:0xf bank_mask:0xf
	v_mul_f32_e32 v59, v59, v247
	v_cvt_pk_bf16_f32 v59, v59, v228
	v_mul_f32_dpp v228, v60, v248 quad_perm:[1,0,3,2] row_mask:0xf bank_mask:0xf
	v_mul_f32_e32 v60, v60, v248
	v_cvt_pk_bf16_f32 v60, v60, v228
	v_mul_f32_dpp v228, v61, v249 quad_perm:[1,0,3,2] row_mask:0xf bank_mask:0xf
	v_mul_f32_e32 v61, v61, v249
	v_cvt_pk_bf16_f32 v61, v61, v228
	v_mul_f32_dpp v228, v62, v250 quad_perm:[1,0,3,2] row_mask:0xf bank_mask:0xf
	v_mul_f32_e32 v62, v62, v250
	v_cvt_pk_bf16_f32 v62, v62, v228
	v_mul_f32_dpp v228, v63, v251 quad_perm:[1,0,3,2] row_mask:0xf bank_mask:0xf
	v_mul_f32_e32 v63, v63, v251
	v_cvt_pk_bf16_f32 v63, v63, v228
	v_mul_f32_dpp v228, v64, v236 quad_perm:[1,0,3,2] row_mask:0xf bank_mask:0xf
	v_mul_f32_e32 v64, v64, v236
	v_cvt_pk_bf16_f32 v64, v64, v228
	v_mul_f32_dpp v228, v65, v237 quad_perm:[1,0,3,2] row_mask:0xf bank_mask:0xf
	v_mul_f32_e32 v65, v65, v237
	v_cvt_pk_bf16_f32 v65, v65, v228
	v_mul_f32_dpp v228, v66, v238 quad_perm:[1,0,3,2] row_mask:0xf bank_mask:0xf
	v_mul_f32_e32 v66, v66, v238
	v_cvt_pk_bf16_f32 v66, v66, v228
	v_mul_f32_dpp v228, v67, v239 quad_perm:[1,0,3,2] row_mask:0xf bank_mask:0xf
	v_mul_f32_e32 v67, v67, v239
	v_cvt_pk_bf16_f32 v67, v67, v228
	v_mul_f32_dpp v228, v68, v240 quad_perm:[1,0,3,2] row_mask:0xf bank_mask:0xf
	v_mul_f32_e32 v68, v68, v240
	v_cvt_pk_bf16_f32 v68, v68, v228
	v_mul_f32_dpp v228, v69, v241 quad_perm:[1,0,3,2] row_mask:0xf bank_mask:0xf
	v_mul_f32_e32 v69, v69, v241
	v_cvt_pk_bf16_f32 v69, v69, v228
	v_mul_f32_dpp v228, v70, v242 quad_perm:[1,0,3,2] row_mask:0xf bank_mask:0xf
	v_mul_f32_e32 v70, v70, v242
	v_cvt_pk_bf16_f32 v70, v70, v228
	v_mul_f32_dpp v228, v71, v243 quad_perm:[1,0,3,2] row_mask:0xf bank_mask:0xf
	v_mul_f32_e32 v71, v71, v243
	v_cvt_pk_bf16_f32 v71, v71, v228
	v_mul_f32_dpp v228, v72, v244 quad_perm:[1,0,3,2] row_mask:0xf bank_mask:0xf
	v_mul_f32_e32 v72, v72, v244
	v_cvt_pk_bf16_f32 v72, v72, v228
	v_mul_f32_dpp v228, v73, v245 quad_perm:[1,0,3,2] row_mask:0xf bank_mask:0xf
	v_mul_f32_e32 v73, v73, v245
	v_cvt_pk_bf16_f32 v73, v73, v228
	v_mul_f32_dpp v228, v74, v246 quad_perm:[1,0,3,2] row_mask:0xf bank_mask:0xf
	v_mul_f32_e32 v74, v74, v246
	v_cvt_pk_bf16_f32 v74, v74, v228
	v_mul_f32_dpp v228, v75, v247 quad_perm:[1,0,3,2] row_mask:0xf bank_mask:0xf
	v_mul_f32_e32 v75, v75, v247
	v_cvt_pk_bf16_f32 v75, v75, v228
	v_mul_f32_dpp v228, v76, v248 quad_perm:[1,0,3,2] row_mask:0xf bank_mask:0xf
	v_mul_f32_e32 v76, v76, v248
	v_cvt_pk_bf16_f32 v76, v76, v228
	v_mul_f32_dpp v228, v77, v249 quad_perm:[1,0,3,2] row_mask:0xf bank_mask:0xf
	v_mul_f32_e32 v77, v77, v249
	v_cvt_pk_bf16_f32 v77, v77, v228
	v_mul_f32_dpp v228, v78, v250 quad_perm:[1,0,3,2] row_mask:0xf bank_mask:0xf
	v_mul_f32_e32 v78, v78, v250
	v_cvt_pk_bf16_f32 v78, v78, v228
	v_mul_f32_dpp v228, v79, v251 quad_perm:[1,0,3,2] row_mask:0xf bank_mask:0xf
	v_mul_f32_e32 v79, v79, v251
	v_cvt_pk_bf16_f32 v79, v79, v228
	v_mul_f32_dpp v228, v80, v236 quad_perm:[1,0,3,2] row_mask:0xf bank_mask:0xf
	v_mul_f32_e32 v80, v80, v236
	v_cvt_pk_bf16_f32 v80, v80, v228
	v_mul_f32_dpp v228, v81, v237 quad_perm:[1,0,3,2] row_mask:0xf bank_mask:0xf
	v_mul_f32_e32 v81, v81, v237
	v_cvt_pk_bf16_f32 v81, v81, v228
	v_mul_f32_dpp v228, v82, v238 quad_perm:[1,0,3,2] row_mask:0xf bank_mask:0xf
	v_mul_f32_e32 v82, v82, v238
	v_cvt_pk_bf16_f32 v82, v82, v228
	v_mul_f32_dpp v228, v83, v239 quad_perm:[1,0,3,2] row_mask:0xf bank_mask:0xf
	v_mul_f32_e32 v83, v83, v239
	v_cvt_pk_bf16_f32 v83, v83, v228
	v_mul_f32_dpp v228, v84, v240 quad_perm:[1,0,3,2] row_mask:0xf bank_mask:0xf
	v_mul_f32_e32 v84, v84, v240
	v_cvt_pk_bf16_f32 v84, v84, v228
	v_mul_f32_dpp v228, v85, v241 quad_perm:[1,0,3,2] row_mask:0xf bank_mask:0xf
	v_mul_f32_e32 v85, v85, v241
	v_cvt_pk_bf16_f32 v85, v85, v228
	v_mul_f32_dpp v228, v86, v242 quad_perm:[1,0,3,2] row_mask:0xf bank_mask:0xf
	v_mul_f32_e32 v86, v86, v242
	v_cvt_pk_bf16_f32 v86, v86, v228
	v_mul_f32_dpp v228, v87, v243 quad_perm:[1,0,3,2] row_mask:0xf bank_mask:0xf
	v_mul_f32_e32 v87, v87, v243
	v_cvt_pk_bf16_f32 v87, v87, v228
	v_mul_f32_dpp v228, v88, v244 quad_perm:[1,0,3,2] row_mask:0xf bank_mask:0xf
	v_mul_f32_e32 v88, v88, v244
	v_cvt_pk_bf16_f32 v88, v88, v228
	v_mul_f32_dpp v228, v89, v245 quad_perm:[1,0,3,2] row_mask:0xf bank_mask:0xf
	v_mul_f32_e32 v89, v89, v245
	v_cvt_pk_bf16_f32 v89, v89, v228
	v_mul_f32_dpp v228, v90, v246 quad_perm:[1,0,3,2] row_mask:0xf bank_mask:0xf
	v_mul_f32_e32 v90, v90, v246
	v_cvt_pk_bf16_f32 v90, v90, v228
	v_mul_f32_dpp v228, v91, v247 quad_perm:[1,0,3,2] row_mask:0xf bank_mask:0xf
	v_mul_f32_e32 v91, v91, v247
	v_cvt_pk_bf16_f32 v91, v91, v228
	v_mul_f32_dpp v228, v92, v248 quad_perm:[1,0,3,2] row_mask:0xf bank_mask:0xf
	v_mul_f32_e32 v92, v92, v248
	v_cvt_pk_bf16_f32 v92, v92, v228
	v_mul_f32_dpp v228, v93, v249 quad_perm:[1,0,3,2] row_mask:0xf bank_mask:0xf
	v_mul_f32_e32 v93, v93, v249
	v_cvt_pk_bf16_f32 v93, v93, v228
	v_mul_f32_dpp v228, v94, v250 quad_perm:[1,0,3,2] row_mask:0xf bank_mask:0xf
	v_mul_f32_e32 v94, v94, v250
	v_cvt_pk_bf16_f32 v94, v94, v228
	v_mul_f32_dpp v228, v95, v251 quad_perm:[1,0,3,2] row_mask:0xf bank_mask:0xf
	v_mul_f32_e32 v95, v95, v251
	v_cvt_pk_bf16_f32 v95, v95, v228
	v_mul_f32_dpp v228, v98, v236 quad_perm:[1,0,3,2] row_mask:0xf bank_mask:0xf
	v_mul_f32_e32 v98, v98, v236
	v_cvt_pk_bf16_f32 v98, v98, v228
	v_mul_f32_dpp v228, v99, v237 quad_perm:[1,0,3,2] row_mask:0xf bank_mask:0xf
	v_mul_f32_e32 v99, v99, v237
	v_cvt_pk_bf16_f32 v99, v99, v228
	v_mul_f32_dpp v228, v100, v238 quad_perm:[1,0,3,2] row_mask:0xf bank_mask:0xf
	v_mul_f32_e32 v100, v100, v238
	v_cvt_pk_bf16_f32 v100, v100, v228
	v_mul_f32_dpp v228, v101, v239 quad_perm:[1,0,3,2] row_mask:0xf bank_mask:0xf
	v_mul_f32_e32 v101, v101, v239
	v_cvt_pk_bf16_f32 v101, v101, v228
	v_mul_f32_dpp v228, v102, v240 quad_perm:[1,0,3,2] row_mask:0xf bank_mask:0xf
	v_mul_f32_e32 v102, v102, v240
	v_cvt_pk_bf16_f32 v102, v102, v228
	v_mul_f32_dpp v228, v103, v241 quad_perm:[1,0,3,2] row_mask:0xf bank_mask:0xf
	v_mul_f32_e32 v103, v103, v241
	v_cvt_pk_bf16_f32 v103, v103, v228
	v_mul_f32_dpp v228, v104, v242 quad_perm:[1,0,3,2] row_mask:0xf bank_mask:0xf
	v_mul_f32_e32 v104, v104, v242
	v_cvt_pk_bf16_f32 v104, v104, v228
	v_mul_f32_dpp v228, v105, v243 quad_perm:[1,0,3,2] row_mask:0xf bank_mask:0xf
	v_mul_f32_e32 v105, v105, v243
	v_cvt_pk_bf16_f32 v105, v105, v228
	v_mul_f32_dpp v228, v106, v244 quad_perm:[1,0,3,2] row_mask:0xf bank_mask:0xf
	v_mul_f32_e32 v106, v106, v244
	v_cvt_pk_bf16_f32 v106, v106, v228
	v_mul_f32_dpp v228, v107, v245 quad_perm:[1,0,3,2] row_mask:0xf bank_mask:0xf
	v_mul_f32_e32 v107, v107, v245
	v_cvt_pk_bf16_f32 v107, v107, v228
	v_mul_f32_dpp v228, v108, v246 quad_perm:[1,0,3,2] row_mask:0xf bank_mask:0xf
	v_mul_f32_e32 v108, v108, v246
	v_cvt_pk_bf16_f32 v108, v108, v228
	v_mul_f32_dpp v228, v109, v247 quad_perm:[1,0,3,2] row_mask:0xf bank_mask:0xf
	v_mul_f32_e32 v109, v109, v247
	v_cvt_pk_bf16_f32 v109, v109, v228
	v_mul_f32_dpp v228, v110, v248 quad_perm:[1,0,3,2] row_mask:0xf bank_mask:0xf
	v_mul_f32_e32 v110, v110, v248
	v_cvt_pk_bf16_f32 v110, v110, v228
	v_mul_f32_dpp v228, v111, v249 quad_perm:[1,0,3,2] row_mask:0xf bank_mask:0xf
	v_mul_f32_e32 v111, v111, v249
	v_cvt_pk_bf16_f32 v111, v111, v228
	v_mul_f32_dpp v228, v112, v250 quad_perm:[1,0,3,2] row_mask:0xf bank_mask:0xf
	v_mul_f32_e32 v112, v112, v250
	v_cvt_pk_bf16_f32 v112, v112, v228
	v_mul_f32_dpp v228, v113, v251 quad_perm:[1,0,3,2] row_mask:0xf bank_mask:0xf
	v_mul_f32_e32 v113, v113, v251
	v_cvt_pk_bf16_f32 v113, v113, v228
	v_mul_f32_dpp v228, v114, v236 quad_perm:[1,0,3,2] row_mask:0xf bank_mask:0xf
	v_mul_f32_e32 v114, v114, v236
	v_cvt_pk_bf16_f32 v114, v114, v228
	v_mul_f32_dpp v228, v115, v237 quad_perm:[1,0,3,2] row_mask:0xf bank_mask:0xf
	v_mul_f32_e32 v115, v115, v237
	v_cvt_pk_bf16_f32 v115, v115, v228
	v_mul_f32_dpp v228, v116, v238 quad_perm:[1,0,3,2] row_mask:0xf bank_mask:0xf
	v_mul_f32_e32 v116, v116, v238
	v_cvt_pk_bf16_f32 v116, v116, v228
	v_mul_f32_dpp v228, v117, v239 quad_perm:[1,0,3,2] row_mask:0xf bank_mask:0xf
	v_mul_f32_e32 v117, v117, v239
	v_cvt_pk_bf16_f32 v117, v117, v228
	v_mul_f32_dpp v228, v118, v240 quad_perm:[1,0,3,2] row_mask:0xf bank_mask:0xf
	v_mul_f32_e32 v118, v118, v240
	v_cvt_pk_bf16_f32 v118, v118, v228
	v_mul_f32_dpp v228, v119, v241 quad_perm:[1,0,3,2] row_mask:0xf bank_mask:0xf
	v_mul_f32_e32 v119, v119, v241
	v_cvt_pk_bf16_f32 v119, v119, v228
	v_mul_f32_dpp v228, v120, v242 quad_perm:[1,0,3,2] row_mask:0xf bank_mask:0xf
	v_mul_f32_e32 v120, v120, v242
	v_cvt_pk_bf16_f32 v120, v120, v228
	v_mul_f32_dpp v228, v121, v243 quad_perm:[1,0,3,2] row_mask:0xf bank_mask:0xf
	v_mul_f32_e32 v121, v121, v243
	v_cvt_pk_bf16_f32 v121, v121, v228
	v_mul_f32_dpp v228, v122, v244 quad_perm:[1,0,3,2] row_mask:0xf bank_mask:0xf
	v_mul_f32_e32 v122, v122, v244
	v_cvt_pk_bf16_f32 v122, v122, v228
	v_mul_f32_dpp v228, v123, v245 quad_perm:[1,0,3,2] row_mask:0xf bank_mask:0xf
	v_mul_f32_e32 v123, v123, v245
	v_cvt_pk_bf16_f32 v123, v123, v228
	v_mul_f32_dpp v228, v124, v246 quad_perm:[1,0,3,2] row_mask:0xf bank_mask:0xf
	v_mul_f32_e32 v124, v124, v246
	v_cvt_pk_bf16_f32 v124, v124, v228
	v_mul_f32_dpp v228, v125, v247 quad_perm:[1,0,3,2] row_mask:0xf bank_mask:0xf
	v_mul_f32_e32 v125, v125, v247
	v_cvt_pk_bf16_f32 v125, v125, v228
	v_mul_f32_dpp v228, v126, v248 quad_perm:[1,0,3,2] row_mask:0xf bank_mask:0xf
	v_mul_f32_e32 v126, v126, v248
	v_cvt_pk_bf16_f32 v126, v126, v228
	v_mul_f32_dpp v228, v127, v249 quad_perm:[1,0,3,2] row_mask:0xf bank_mask:0xf
	v_mul_f32_e32 v127, v127, v249
	v_cvt_pk_bf16_f32 v127, v127, v228
	v_mul_f32_dpp v228, v128, v250 quad_perm:[1,0,3,2] row_mask:0xf bank_mask:0xf
	v_mul_f32_e32 v128, v128, v250
	v_cvt_pk_bf16_f32 v128, v128, v228
	v_mul_f32_dpp v228, v129, v251 quad_perm:[1,0,3,2] row_mask:0xf bank_mask:0xf
	v_mul_f32_e32 v129, v129, v251
	v_cvt_pk_bf16_f32 v129, v129, v228
	s_mov_b64 s[48:49], exec
	s_mov_b32 s50, 0x55555555
	s_mov_b32 s51, 0x55555555
	s_mov_b64 exec, s[50:51]
	global_store_dword v233, v0, s[42:43] offset:0
	global_store_dword v233, v1, s[42:43] offset:256
	global_store_dword v233, v2, s[42:43] offset:512
	global_store_dword v233, v3, s[42:43] offset:768
	global_store_dword v233, v4, s[42:43] offset:2048
	global_store_dword v233, v5, s[42:43] offset:2304
	global_store_dword v233, v6, s[42:43] offset:2560
	global_store_dword v233, v7, s[42:43] offset:2816
	global_store_dword v234, v8, s[42:43] offset:0
	global_store_dword v234, v9, s[42:43] offset:256
	global_store_dword v234, v10, s[42:43] offset:512
	global_store_dword v234, v11, s[42:43] offset:768
	global_store_dword v234, v12, s[42:43] offset:2048
	global_store_dword v234, v13, s[42:43] offset:2304
	global_store_dword v234, v14, s[42:43] offset:2560
	global_store_dword v234, v15, s[42:43] offset:2816
	global_store_dword v233, v16, s[42:43] offset:64
	global_store_dword v233, v17, s[42:43] offset:320
	global_store_dword v233, v18, s[42:43] offset:576
	global_store_dword v233, v19, s[42:43] offset:832
	global_store_dword v233, v20, s[42:43] offset:2112
	global_store_dword v233, v21, s[42:43] offset:2368
	global_store_dword v233, v22, s[42:43] offset:2624
	global_store_dword v233, v23, s[42:43] offset:2880
	global_store_dword v234, v24, s[42:43] offset:64
	global_store_dword v234, v25, s[42:43] offset:320
	global_store_dword v234, v26, s[42:43] offset:576
	global_store_dword v234, v27, s[42:43] offset:832
	global_store_dword v234, v28, s[42:43] offset:2112
	global_store_dword v234, v29, s[42:43] offset:2368
	global_store_dword v234, v30, s[42:43] offset:2624
	global_store_dword v234, v31, s[42:43] offset:2880
	global_store_dword v233, v32, s[42:43] offset:128
	global_store_dword v233, v33, s[42:43] offset:384
	global_store_dword v233, v34, s[42:43] offset:640
	global_store_dword v233, v35, s[42:43] offset:896
	global_store_dword v233, v36, s[42:43] offset:2176
	global_store_dword v233, v37, s[42:43] offset:2432
	global_store_dword v233, v38, s[42:43] offset:2688
	global_store_dword v233, v39, s[42:43] offset:2944
	global_store_dword v234, v40, s[42:43] offset:128
	global_store_dword v234, v41, s[42:43] offset:384
	global_store_dword v234, v42, s[42:43] offset:640
	global_store_dword v234, v43, s[42:43] offset:896
	global_store_dword v234, v44, s[42:43] offset:2176
	global_store_dword v234, v45, s[42:43] offset:2432
	global_store_dword v234, v46, s[42:43] offset:2688
	global_store_dword v234, v47, s[42:43] offset:2944
	global_store_dword v233, v48, s[42:43] offset:192
	global_store_dword v233, v49, s[42:43] offset:448
	global_store_dword v233, v50, s[42:43] offset:704
	global_store_dword v233, v51, s[42:43] offset:960
	global_store_dword v233, v52, s[42:43] offset:2240
	global_store_dword v233, v53, s[42:43] offset:2496
	global_store_dword v233, v54, s[42:43] offset:2752
	global_store_dword v233, v55, s[42:43] offset:3008
	global_store_dword v234, v56, s[42:43] offset:192
	global_store_dword v234, v57, s[42:43] offset:448
	global_store_dword v234, v58, s[42:43] offset:704
	global_store_dword v234, v59, s[42:43] offset:960
	global_store_dword v234, v60, s[42:43] offset:2240
	global_store_dword v234, v61, s[42:43] offset:2496
	global_store_dword v234, v62, s[42:43] offset:2752
	global_store_dword v234, v63, s[42:43] offset:3008
	global_store_dword v233, v64, s[44:45] offset:0
	global_store_dword v233, v65, s[44:45] offset:256
	global_store_dword v233, v66, s[44:45] offset:512
	global_store_dword v233, v67, s[44:45] offset:768
	global_store_dword v233, v68, s[44:45] offset:2048
	global_store_dword v233, v69, s[44:45] offset:2304
	global_store_dword v233, v70, s[44:45] offset:2560
	global_store_dword v233, v71, s[44:45] offset:2816
	global_store_dword v234, v72, s[44:45] offset:0
	global_store_dword v234, v73, s[44:45] offset:256
	global_store_dword v234, v74, s[44:45] offset:512
	global_store_dword v234, v75, s[44:45] offset:768
	global_store_dword v234, v76, s[44:45] offset:2048
	global_store_dword v234, v77, s[44:45] offset:2304
	global_store_dword v234, v78, s[44:45] offset:2560
	global_store_dword v234, v79, s[44:45] offset:2816
	global_store_dword v233, v80, s[44:45] offset:64
	global_store_dword v233, v81, s[44:45] offset:320
	global_store_dword v233, v82, s[44:45] offset:576
	global_store_dword v233, v83, s[44:45] offset:832
	global_store_dword v233, v84, s[44:45] offset:2112
	global_store_dword v233, v85, s[44:45] offset:2368
	global_store_dword v233, v86, s[44:45] offset:2624
	global_store_dword v233, v87, s[44:45] offset:2880
	global_store_dword v234, v88, s[44:45] offset:64
	global_store_dword v234, v89, s[44:45] offset:320
	global_store_dword v234, v90, s[44:45] offset:576
	global_store_dword v234, v91, s[44:45] offset:832
	global_store_dword v234, v92, s[44:45] offset:2112
	global_store_dword v234, v93, s[44:45] offset:2368
	global_store_dword v234, v94, s[44:45] offset:2624
	global_store_dword v234, v95, s[44:45] offset:2880
	global_store_dword v233, v98, s[44:45] offset:128
	global_store_dword v233, v99, s[44:45] offset:384
	global_store_dword v233, v100, s[44:45] offset:640
	global_store_dword v233, v101, s[44:45] offset:896
	global_store_dword v233, v102, s[44:45] offset:2176
	global_store_dword v233, v103, s[44:45] offset:2432
	global_store_dword v233, v104, s[44:45] offset:2688
	global_store_dword v233, v105, s[44:45] offset:2944
	global_store_dword v234, v106, s[44:45] offset:128
	global_store_dword v234, v107, s[44:45] offset:384
	global_store_dword v234, v108, s[44:45] offset:640
	global_store_dword v234, v109, s[44:45] offset:896
	global_store_dword v234, v110, s[44:45] offset:2176
	global_store_dword v234, v111, s[44:45] offset:2432
	global_store_dword v234, v112, s[44:45] offset:2688
	global_store_dword v234, v113, s[44:45] offset:2944
	global_store_dword v233, v114, s[44:45] offset:192
	global_store_dword v233, v115, s[44:45] offset:448
	global_store_dword v233, v116, s[44:45] offset:704
	global_store_dword v233, v117, s[44:45] offset:960
	global_store_dword v233, v118, s[44:45] offset:2240
	global_store_dword v233, v119, s[44:45] offset:2496
	global_store_dword v233, v120, s[44:45] offset:2752
	global_store_dword v233, v121, s[44:45] offset:3008
	global_store_dword v234, v122, s[44:45] offset:192
	global_store_dword v234, v123, s[44:45] offset:448
	global_store_dword v234, v124, s[44:45] offset:704
	global_store_dword v234, v125, s[44:45] offset:960
	global_store_dword v234, v126, s[44:45] offset:2240
	global_store_dword v234, v127, s[44:45] offset:2496
	global_store_dword v234, v128, s[44:45] offset:2752
	global_store_dword v234, v129, s[44:45] offset:3008
	s_mov_b64 exec, s[48:49]
	s_add_i32 s9, s9, 1
	s_cmp_lt_u32 s9, 4
	s_cbranch_scc1 .Lfa_block
	s_add_i32 s2, s2, s7
	s_branch .Lfa_task
.Lfa_done:
	s_waitcnt vmcnt(0) lgkmcnt(0)
	v_mbcnt_lo_u32_b32 v0, -1, 0
	v_mbcnt_hi_u32_b32 v0, -1, v0
	s_mul_i32 s21, s15, 0xc00
	s_add_i32 s21, s21, 0x18800
	v_lshlrev_b32_e32 v1, 2, v0
	v_add_u32_e32 v1, s21, v1
	ds_read_b32 v162, v1 offset:0
	ds_read_b32 v163, v1 offset:256
	ds_read_b32 v164, v1 offset:512
	ds_read_b32 v165, v1 offset:768
	ds_read_b32 v166, v1 offset:1024
	ds_read_b32 v167, v1 offset:1280
	ds_read_b32 v168, v1 offset:1536
	ds_read_b32 v169, v1 offset:1792
	ds_read_b32 v170, v1 offset:2048
	ds_read_b32 v171, v1 offset:2304
	ds_read_b32 v172, v1 offset:2560
	ds_read_b32 v173, v1 offset:2816
	v_mov_b32_e32 v214, 0x3f4ccccd
	v_mov_b32_e32 v215, 0xff800000
	v_mov_b32_e32 v216, 0xbf3a00e3
	v_mov_b32_e32 v217, 0x3a000000
	v_mov_b32_e32 v218, 0xf149f2ca
	v_mov_b32_e32 v219, 0x7f800000
	v_mov_b32_e32 v220, 0x3fb8aa3b
	v_mov_b32_e32 v221, 0x32a5705f
	v_mov_b32_e32 v222, 0xc2ce8ed0
	v_mov_b32_e32 v223, 0x42b17218
	v_mov_b32_e32 v224, 0x3b800000
	v_mov_b32_e32 v225, 0x41b17218
	v_mov_b32_e32 v226, 0x4200
	v_mov_b32_e32 v227, 0x34000
	s_waitcnt lgkmcnt(0)
